# memory-side cache protection: the lightly loaded XCD groups (and the all-share fallback) now run the layer-1 conversion between E1 and E2 instead of after E2, so its ~300 MB of traffic no longer evict
# baseline (speedup 1.0000x reference)
;     __device__ bool next(int i, Unit& u) const {
;         const long L = (long)i * G + c; int wgid;
;         if (aligned) {
;             const int ng = (nM + WGM - 1) / WGM, gq = ng / NXCD, gr = ng % NXCD, xcd = (int)(L % NXCD); const long off = L / NXCD;
;             const int g0 = xcd * gq + (xcd < gr ? xcd : gr), g1 = g0 + gq + (xcd < gr ? 1 : 0);
;             const long w = (long)g0 * (WGM * 4) + off, wend = (long)g1 * (WGM * 4) < nwg ? (long)g1 * (WGM * 4) : nwg;
;             if (w >= wend) return false;
;             wgid = (int)w;
; __global__ void __launch_bounds__(NWAVES * 64, 2) mk_fwd(Args args) {
;     ...
;         {
;             const int step = G * NWAVES; int it0 = CONV_EARLY + bid * NWAVES + wave;
;             ConvDesc dA, dB; f32x4 vA[16], vB[16];
;             if (it0 < NCONV_ITEMS) { CONV_DECODE(dA, it0); conv_load(vA, dA, lane); }
; #pragma unroll 1
;             for (; it0 < NCONV_ITEMS; it0 += 2 * step) {
;                 const bool hasB = it0 + step < NCONV_ITEMS, hasA2 = it0 + 2 * step < NCONV_ITEMS;
;                 if (hasB) { CONV_DECODE(dB, it0 + step); conv_load(vB, dB, lane); }
;                 conv_process(vA, dA, scr, lane);
;                 if (hasA2) { CONV_DECODE(dA, it0 + 2 * step); conv_load(vA, dA, lane); }
;                 if (hasB) conv_process(vB, dB, scr, lane);
;             }
.LBB0_1541:
	v_mov_b32_e32 v252, 0x27c80
	ds_read_b32 v252, v252
	s_waitcnt lgkmcnt(0)
	v_readfirstlane_b32 s100, v252
	s_nop 1
	s_lshr_b32 s100, s100, 8
	s_add_i32 s100, s100, 3
	s_lshr_b32 s100, s100, 2
	s_and_b32 s100, s100, 7
	s_and_b32 s98, s83, 7
	s_cmp_eq_u32 s100, 0
	s_cbranch_scc1 .LslotA_all
	s_cmp_ge_u32 s100, 6
	s_cbranch_scc1 .LslotA_all
	s_lshr_b32 s101, s83, 3
	s_cmp_lt_u32 s98, s100
	s_cbranch_scc1 .LslotA_heavy
	s_sub_i32 s98, s98, s100
	s_lshl_b32 s98, s98, 5
	s_add_i32 s98, s98, s101
	s_lshl_b32 s101, s100, 6
	s_add_i32 s98, s98, s101
	s_lshl_b32 s101, s100, 5
	s_add_i32 s98, s98, s101
	s_sub_i32 s100, 8, s100
	s_lshl_b32 s100, s100, 5
	s_add_i32 s98, s98, 0x600
	s_mov_b32 s101, 0x6900
	s_branch .LslotA_go
.LslotA_heavy:
	s_cmp_lt_u32 s101, 16
	s_cbranch_scc1 .LslotA_skip
	s_lshl_b32 s98, s98, 4
	s_add_i32 s98, s98, s101
	s_sub_i32 s98, s98, 16
	s_lshl_b32 s100, s100, 4
	s_add_i32 s98, s98, 0x600
	s_lshl_b32 s101, s100, 5
	s_add_i32 s101, s101, 0x3900
	s_branch .LslotA_go
.LslotA_all:
	s_add_i32 s98, s83, 0x600
	s_mov_b32 s100, s33
	s_mov_b32 s101, 0x6900
.LslotA_go:
	v_writelane_b32 v253, s14, 0
	v_writelane_b32 v253, s15, 1
	v_writelane_b32 v253, s16, 2
	v_writelane_b32 v253, s17, 3
	v_writelane_b32 v253, s19, 4
	v_writelane_b32 v253, s21, 5
	v_writelane_b32 v253, s57, 6
	v_mov_b32_e32 v254, v3
	s_mov_b32 s99, 5
	s_lshl_b32 s50, s98, 3
	s_add_i32 s50, s50, s85
	s_lshl_b32 s49, s98, 9
	s_lshl_b32 s48, s100, 3
	s_lshl_b32 s2, s100, 9
	s_mov_b64 s[0:1], s[78:79]
	s_mul_i32 s3, s85, 0x4100
	s_lshl_b32 s88, s85, 6
	s_branch .Lconv_entry

;     __device__ bool next(int i, Unit& u) const {
;         const long L = (long)i * G + c; int wgid;
;         if (aligned) {
;             const int ng = (nM + WGM - 1) / WGM, gq = ng / NXCD, gr = ng % NXCD, xcd = (int)(L % NXCD); const long off = L / NXCD;
;             const int g0 = xcd * gq + (xcd < gr ? xcd : gr), g1 = g0 + gq + (xcd < gr ? 1 : 0);
;             const long w = (long)g0 * (WGM * 4) + off, wend = (long)g1 * (WGM * 4) < nwg ? (long)g1 * (WGM * 4) : nwg;
;             if (w >= wend) return false;
;             wgid = (int)w;
; __global__ void __launch_bounds__(NWAVES * 64, 2) mk_fwd(Args args) {
;     ...
;         {
;             const int step = G * NWAVES; int it0 = CONV_EARLY + bid * NWAVES + wave;
;             ConvDesc dA, dB; f32x4 vA[16], vB[16];
;             if (it0 < NCONV_ITEMS) { CONV_DECODE(dA, it0); conv_load(vA, dA, lane); }
; #pragma unroll 1
;             for (; it0 < NCONV_ITEMS; it0 += 2 * step) {
;                 const bool hasB = it0 + step < NCONV_ITEMS, hasA2 = it0 + 2 * step < NCONV_ITEMS;
;                 if (hasB) { CONV_DECODE(dB, it0 + step); conv_load(vB, dB, lane); }
;                 conv_process(vA, dA, scr, lane);
;                 if (hasA2) { CONV_DECODE(dA, it0 + 2 * step); conv_load(vA, dA, lane); }
;                 if (hasB) conv_process(vB, dB, scr, lane);
;             }
.LBB0_1657:
	s_waitcnt vmcnt(0) lgkmcnt(0)
	s_barrier
	v_mov_b32_e32 v252, 0x27c80
	ds_read_b32 v252, v252
	s_waitcnt lgkmcnt(0)
	v_readfirstlane_b32 s100, v252
	s_nop 1
	s_lshr_b32 s100, s100, 8
	s_add_i32 s100, s100, 3
	s_lshr_b32 s100, s100, 2
	s_and_b32 s100, s100, 7
	s_and_b32 s98, s83, 7
	s_cmp_eq_u32 s100, 0
	s_cbranch_scc1 .Lq_done
	s_cmp_ge_u32 s100, 6
	s_cbranch_scc1 .Lq_done
	s_lshr_b32 s101, s83, 3
	s_cmp_ge_u32 s98, s100
	s_cbranch_scc1 .Lq_done
	s_cmp_lt_u32 s101, 16
	s_cbranch_scc1 .Lq_done
	s_lshl_b32 s98, s98, 4
	s_add_i32 s98, s98, s101
	s_sub_i32 s98, s98, 16
	s_lshl_b32 s100, s100, 4
	s_lshl_b32 s101, s100, 2
	s_add_i32 s98, s98, s101
	s_add_i32 s98, s98, 0x600
	s_lshl_b32 s101, s100, 5
	s_lshl_b32 s99, s100, 4
	s_add_i32 s101, s101, s99
	s_add_i32 s101, s101, 0x3900
	s_mov_b32 s99, 2
	s_lshl_b32 s50, s98, 3
	s_add_i32 s50, s50, s85
	s_lshl_b32 s49, s98, 9
	s_lshl_b32 s48, s100, 3
	s_lshl_b32 s2, s100, 9
	s_mov_b64 s[0:1], s[78:79]
	s_mul_i32 s3, s85, 0x4100
	s_lshl_b32 s88, s85, 6
	s_branch .Lconv_entry
